# layer kernels: kernarg pointer loads and the eps scalar issued together at entry (one scalar-cache miss instead of a serialized chain)
# speedup vs baseline: 1.0355x; 1.0054x over previous
_Z12layer_kernelILb1ELi512ELi64EEvPKDv8_DF16_PKfPS0_PiS6_S6_S2_S4_S5_PfPK15HIP_vector_typeIiLj2EEPKi:
	s_load_dword s3, s[0:1], 0x60
	s_load_dwordx2 s[4:5], s[0:1], 0x58
	s_load_dwordx2 s[44:45], s[0:1], 0x38
	s_load_dwordx2 s[24:25], s[0:1], 0x0
	s_waitcnt lgkmcnt(0)
	s_ashr_i32 s6, s3, 3
	s_and_b32 s7, s3, 7
	s_and_b32 s3, s2, 7
	s_add_i32 s10, s6, 1
	s_cmp_ge_u32 s3, s7
	s_cbranch_scc0 .LBB4_2
	s_mul_i32 s8, s10, s7
	s_sub_i32 s7, s3, s7
	s_mul_i32 s7, s7, s6
	s_add_i32 s11, s8, s7
	s_cbranch_execz .LBB4_3
	s_branch .LBB4_4
.LBB4_2:
.LBB4_3:
	s_mul_i32 s11, s10, s3
.LBB4_4:
	s_mov_b64 s[6:7], s[44:45]
	s_ashr_i32 s2, s2, 3
	s_add_i32 s14, s11, s2
	v_lshrrev_b32_e32 v31, 3, v0
	s_lshl_b32 s30, s14, 6
	v_and_b32_e32 v44, 62, v31
	v_or_b32_e32 v11, s30, v44
	v_min_i32_e32 v2, 0x1869f, v11
	v_ashrrev_i32_e32 v3, 31, v2
	v_and_b32_e32 v42, 15, v0
	v_lshlrev_b64 v[2:3], 8, v[2:3]
	v_mov_b32_e32 v27, 0
	s_waitcnt lgkmcnt(0)
	v_lshl_add_u64 v[2:3], s[24:25], 0, v[2:3]
	v_lshlrev_b32_e32 v26, 4, v42
	v_lshl_add_u64 v[2:3], v[2:3], 0, v[26:27]
	global_load_dwordx4 v[18:21], v[2:3], off
	s_ashr_i32 s15, s14, 31
	s_lshl_b64 s[2:3], s[14:15], 2
	s_add_u32 s2, s4, s2
	s_addc_u32 s3, s5, s3
	s_load_dwordx2 s[26:27], s[0:1], 0x50
	s_load_dwordx2 s[20:21], s[2:3], 0x0
	v_cmp_gt_u32_e64 s[2:3], 64, v0
	s_and_saveexec_b64 s[4:5], s[2:3]
	v_lshlrev_b32_e32 v1, 2, v0
	ds_write_b32 v1, v27 offset:25872
	s_or_b64 exec, exec, s[4:5]
	s_load_dwordx2 s[16:17], s[0:1], 0x48
	s_load_dwordx4 s[8:11], s[0:1], 0x18
	s_load_dwordx2 s[18:19], s[0:1], 0x30
	s_load_dword s31, s[6:7], 0x0
	s_waitcnt lgkmcnt(0)
	v_add_u32_e32 v2, s20, v0
	v_cmp_gt_i32_e32 vcc, s21, v2
	v_ashrrev_i32_e32 v3, 31, v2
	s_barrier
	s_and_saveexec_b64 s[6:7], vcc
	s_cbranch_execz .LBB4_9
	v_lshl_add_u64 v[4:5], v[2:3], 3, s[26:27]
	s_mov_b64 s[12:13], 0
	v_mov_b32_e32 v1, 1
	s_mov_b64 s[22:23], 0x1000
	v_mov_b32_e32 v6, v2

_Z12layer_kernelILb0ELi256ELi32EEvPKDv8_DF16_PKfPS0_PiS6_S6_S2_S4_S5_PfPK15HIP_vector_typeIiLj2EEPKi:
	s_load_dword s3, s[0:1], 0x60
	s_load_dwordx2 s[26:27], s[0:1], 0x38
	s_load_dwordx2 s[28:29], s[0:1], 0x0
	s_load_dwordx2 s[14:15], s[0:1], 0x20
	s_load_dwordx2 s[8:9], s[0:1], 0x18
	s_waitcnt lgkmcnt(0)
	s_load_dword s16, s[26:27], 0x0
	s_ashr_i32 s4, s3, 3
	s_and_b32 s5, s3, 7
	s_and_b32 s3, s2, 7
	s_add_i32 s10, s4, 1
	s_cmp_ge_u32 s3, s5
	s_cbranch_scc0 .LBB5_2
	s_mul_i32 s6, s10, s5
	s_sub_i32 s5, s3, s5
	s_mul_i32 s5, s5, s4
	s_add_i32 s11, s6, s5
	s_cbranch_execz .LBB5_3
	s_branch .LBB5_4

.LBB5_4:
	s_mov_b64 s[4:5], s[28:29]
	s_ashr_i32 s2, s2, 3
	s_add_i32 s25, s11, s2
	v_lshrrev_b32_e32 v35, 3, v0
	s_lshl_b32 s24, s25, 5
	v_and_b32_e32 v60, 30, v35
	v_or_b32_e32 v8, s24, v60
	v_min_i32_e32 v2, 0x1869f, v8
	v_ashrrev_i32_e32 v3, 31, v2
	v_and_b32_e32 v1, 15, v0
	v_lshlrev_b64 v[2:3], 8, v[2:3]
	v_mov_b32_e32 v27, 0
	v_lshl_add_u64 v[2:3], s[4:5], 0, v[2:3]
	v_lshlrev_b32_e32 v26, 4, v1
	v_lshl_add_u64 v[2:3], v[2:3], 0, v[26:27]
	global_load_dwordx4 v[2:5], v[2:3], off
	v_cmp_gt_u32_e32 vcc, 33, v0
	s_and_saveexec_b64 s[2:3], vcc
	s_cbranch_execz .LBB5_6
	v_add_u32_e32 v6, s24, v0
	v_min_i32_e32 v6, 0x186a0, v6
	v_ashrrev_i32_e32 v7, 31, v6
	v_lshl_add_u64 v[6:7], v[6:7], 2, s[8:9]
	global_load_dword v6, v[6:7], off
	v_lshlrev_b32_e32 v7, 2, v0
	s_waitcnt vmcnt(0)
	ds_write_b32 v7, v6 offset:12800
.LBB5_6:
	s_or_b64 exec, exec, s[2:3]
	s_movk_i32 s2, 0x3000
	v_add_u32_e64 v6, s2, 0
	s_waitcnt lgkmcnt(0)
	s_barrier
	ds_read2_b32 v[28:29], v6 offset0:128 offset1:160
	s_load_dwordx2 s[8:9], s[0:1], 0x48
	s_load_dwordx2 s[10:11], s[0:1], 0x30
	s_waitcnt lgkmcnt(0)
	v_sub_u32_e32 v6, v29, v28
	v_cmp_gt_i32_e32 vcc, v6, v0
	s_and_saveexec_b64 s[2:3], vcc
	s_cbranch_execz .LBB5_9
	v_min_i32_e32 v9, 0x400, v6
	v_add_u32_e32 v6, v0, v28
	v_ashrrev_i32_e32 v7, 31, v6
	v_mov_b32_e32 v10, 0x2200
	v_lshl_add_u64 v[6:7], v[6:7], 2, s[14:15]
	v_lshl_add_u32 v10, v0, 2, v10
	s_mov_b64 s[6:7], 0
	s_mov_b64 s[12:13], 0x400
	v_mov_b32_e32 v11, v0

	.amdhsa_kernel _Z12layer_kernelILb0ELi256ELi32EEvPKDv8_DF16_PKfPS0_PiS6_S6_S2_S4_S5_PfPK15HIP_vector_typeIiLj2EEPKi
		.amdhsa_group_segment_fixed_size 12932
		.amdhsa_private_segment_fixed_size 0
		.amdhsa_kernarg_size 352
		.amdhsa_user_sgpr_count 2
		.amdhsa_user_sgpr_dispatch_ptr 0
		.amdhsa_user_sgpr_queue_ptr 0
		.amdhsa_user_sgpr_kernarg_segment_ptr 1
		.amdhsa_user_sgpr_dispatch_id 0
		.amdhsa_user_sgpr_kernarg_preload_length 0
		.amdhsa_user_sgpr_kernarg_preload_offset 0
		.amdhsa_user_sgpr_private_segment_size 0
		.amdhsa_uses_dynamic_stack 0
		.amdhsa_enable_private_segment 0
		.amdhsa_system_sgpr_workgroup_id_x 1
		.amdhsa_system_sgpr_workgroup_id_y 0
		.amdhsa_system_sgpr_workgroup_id_z 0
		.amdhsa_system_sgpr_workgroup_info 0
		.amdhsa_system_vgpr_workitem_id 0
		.amdhsa_next_free_vgpr 64
		.amdhsa_next_free_sgpr 30
		.amdhsa_accum_offset 64
		.amdhsa_reserve_vcc 1
		.amdhsa_float_round_mode_32 0
		.amdhsa_float_round_mode_16_64 0
		.amdhsa_float_denorm_mode_32 3
		.amdhsa_float_denorm_mode_16_64 3
		.amdhsa_dx10_clamp 1
		.amdhsa_ieee_mode 1
		.amdhsa_fp16_overflow 0
		.amdhsa_tg_split 0
		.amdhsa_exception_fp_ieee_invalid_op 0
		.amdhsa_exception_fp_denorm_src 0
		.amdhsa_exception_fp_ieee_div_zero 0
		.amdhsa_exception_fp_ieee_overflow 0
		.amdhsa_exception_fp_ieee_underflow 0
		.amdhsa_exception_fp_ieee_inexact 0
		.amdhsa_exception_int_div_zero 0
	.end_amdhsa_kernel

amdhsa.kernels:
  - .agpr_count:     0
    .args:
      - .actual_access:  read_only
        .address_space:  global
        .offset:         0
        .size:           8
        .value_kind:     global_buffer
      - .address_space:  global
        .offset:         8
        .size:           8
        .value_kind:     global_buffer
      - .actual_access:  read_only
        .address_space:  global
        .offset:         16
        .size:           8
        .value_kind:     global_buffer
      - .actual_access:  read_only
        .address_space:  global
        .offset:         24
        .size:           8
        .value_kind:     global_buffer
      - .actual_access:  write_only
        .address_space:  global
        .offset:         32
        .size:           8
        .value_kind:     global_buffer
      - .actual_access:  read_only
        .address_space:  global
        .offset:         40
        .size:           8
        .value_kind:     global_buffer
      - .actual_access:  write_only
        .address_space:  global
        .offset:         48
        .size:           8
        .value_kind:     global_buffer
      - .actual_access:  write_only
        .address_space:  global
        .offset:         56
        .size:           8
        .value_kind:     global_buffer
    .group_segment_fixed_size: 6400
    .kernarg_segment_align: 8
    .kernarg_segment_size: 64
    .language:       OpenCL C
    .language_version:
      - 2
      - 0
    .max_flat_workgroup_size: 1024
    .name:           _Z17prep_count_kernelPKfPDv8_DF16_S0_S0_S2_PKiPiP15HIP_vector_typeIfLj4EE
    .private_segment_fixed_size: 0
    .sgpr_count:     22
    .sgpr_spill_count: 0
    .symbol:         _Z17prep_count_kernelPKfPDv8_DF16_S0_S0_S2_PKiPiP15HIP_vector_typeIfLj4EE.kd
    .uniform_work_group_size: 1
    .uses_dynamic_stack: false
    .vgpr_count:     22
    .vgpr_spill_count: 0
    .wavefront_size: 64
  - .agpr_count:     0
    .args:
      - .actual_access:  read_only
        .address_space:  global
        .offset:         0
        .size:           8
        .value_kind:     global_buffer
      - .actual_access:  read_only
        .address_space:  global
        .offset:         8
        .size:           8
        .value_kind:     global_buffer
      - .actual_access:  read_only
        .address_space:  global
        .offset:         16
        .size:           8
        .value_kind:     global_buffer
      - .actual_access:  write_only
        .address_space:  global
        .offset:         24
        .size:           8
        .value_kind:     global_buffer
      - .actual_access:  write_only
        .address_space:  global
        .offset:         32
        .size:           8
        .value_kind:     global_buffer
    .group_segment_fixed_size: 124704
    .kernarg_segment_align: 8
    .kernarg_segment_size: 40
    .language:       OpenCL C
    .language_version:
      - 2
      - 0
    .max_flat_workgroup_size: 1024
    .name:           _Z14scatter_kernelPKiS0_S0_PiP15HIP_vector_typeIiLj2EE
    .private_segment_fixed_size: 0
    .sgpr_count:     55
    .sgpr_spill_count: 0
    .symbol:         _Z14scatter_kernelPKiS0_S0_PiP15HIP_vector_typeIiLj2EE.kd
    .uniform_work_group_size: 1
    .uses_dynamic_stack: false
    .vgpr_count:     100
    .vgpr_spill_count: 0
    .wavefront_size: 64
  - .agpr_count:     0
    .args:
      - .actual_access:  read_only
        .address_space:  global
        .offset:         0
        .size:           8
        .value_kind:     global_buffer
      - .address_space:  global
        .offset:         8
        .size:           8
        .value_kind:     global_buffer
      - .address_space:  global
        .offset:         16
        .size:           8
        .value_kind:     global_buffer
      - .actual_access:  read_only
        .address_space:  global
        .offset:         24
        .size:           8
        .value_kind:     global_buffer
      - .actual_access:  read_only
        .address_space:  global
        .offset:         32
        .size:           8
        .value_kind:     global_buffer
      - .actual_access:  read_only
        .address_space:  global
        .offset:         40
        .size:           8
        .value_kind:     global_buffer
      - .offset:         48
        .size:           4
        .value_kind:     hidden_block_count_x
      - .offset:         52
        .size:           4
        .value_kind:     hidden_block_count_y
      - .offset:         56
        .size:           4
        .value_kind:     hidden_block_count_z
      - .offset:         60
        .size:           2
        .value_kind:     hidden_group_size_x
      - .offset:         62
        .size:           2
        .value_kind:     hidden_group_size_y
      - .offset:         64
        .size:           2
        .value_kind:     hidden_group_size_z
      - .offset:         66
        .size:           2
        .value_kind:     hidden_remainder_x
      - .offset:         68
        .size:           2
        .value_kind:     hidden_remainder_y
      - .offset:         70
        .size:           2
        .value_kind:     hidden_remainder_z
      - .offset:         88
        .size:           8
        .value_kind:     hidden_global_offset_x
      - .offset:         96
        .size:           8
        .value_kind:     hidden_global_offset_y
      - .offset:         104
        .size:           8
        .value_kind:     hidden_global_offset_z
      - .offset:         112
        .size:           2
        .value_kind:     hidden_grid_dims
    .group_segment_fixed_size: 1024
    .kernarg_segment_align: 8
    .kernarg_segment_size: 304
    .language:       OpenCL C
    .language_version:
      - 2
      - 0
    .max_flat_workgroup_size: 256
    .name:           _Z9bn_kernelPKDv8_DF16_S1_PS_PKfS4_S4_
    .private_segment_fixed_size: 0
    .sgpr_count:     20
    .sgpr_spill_count: 0
    .symbol:         _Z9bn_kernelPKDv8_DF16_S1_PS_PKfS4_S4_.kd
    .uniform_work_group_size: 1
    .uses_dynamic_stack: false
    .vgpr_count:     64
    .vgpr_spill_count: 0
    .wavefront_size: 64
  - .agpr_count:     0
    .args:
      - .actual_access:  read_only
        .address_space:  global
        .offset:         0
        .size:           8
        .value_kind:     global_buffer
      - .actual_access:  read_only
        .address_space:  global
        .offset:         8
        .size:           8
        .value_kind:     global_buffer
      - .actual_access:  read_only
        .address_space:  global
        .offset:         16
        .size:           8
        .value_kind:     global_buffer
      - .actual_access:  read_only
        .address_space:  global
        .offset:         24
        .size:           8
        .value_kind:     global_buffer
      - .actual_access:  read_only
        .address_space:  global
        .offset:         32
        .size:           8
        .value_kind:     global_buffer
      - .actual_access:  read_only
        .address_space:  global
        .offset:         40
        .size:           8
        .value_kind:     global_buffer
      - .actual_access:  read_only
        .address_space:  global
        .offset:         48
        .size:           8
        .value_kind:     global_buffer
      - .actual_access:  write_only
        .address_space:  global
        .offset:         56
        .size:           8
        .value_kind:     global_buffer
      - .offset:         64
        .size:           4
        .value_kind:     hidden_block_count_x
      - .offset:         68
        .size:           4
        .value_kind:     hidden_block_count_y
      - .offset:         72
        .size:           4
        .value_kind:     hidden_block_count_z
      - .offset:         76
        .size:           2
        .value_kind:     hidden_group_size_x
      - .offset:         78
        .size:           2
        .value_kind:     hidden_group_size_y
      - .offset:         80
        .size:           2
        .value_kind:     hidden_group_size_z
      - .offset:         82
        .size:           2
        .value_kind:     hidden_remainder_x
      - .offset:         84
        .size:           2
        .value_kind:     hidden_remainder_y
      - .offset:         86
        .size:           2
        .value_kind:     hidden_remainder_z
      - .offset:         104
        .size:           8
        .value_kind:     hidden_global_offset_x
      - .offset:         112
        .size:           8
        .value_kind:     hidden_global_offset_y
      - .offset:         120
        .size:           8
        .value_kind:     hidden_global_offset_z
      - .offset:         128
        .size:           2
        .value_kind:     hidden_grid_dims
    .group_segment_fixed_size: 34816
    .kernarg_segment_align: 8
    .kernarg_segment_size: 320
    .language:       OpenCL C
    .language_version:
      - 2
      - 0
    .max_flat_workgroup_size: 512
    .name:           _Z12final_kernelPKDv8_DF16_S1_PKfS3_S3_S1_S3_Pf
    .private_segment_fixed_size: 0
    .sgpr_count:     28
    .sgpr_spill_count: 0
    .symbol:         _Z12final_kernelPKDv8_DF16_S1_PKfS3_S3_S1_S3_Pf.kd
    .uniform_work_group_size: 1
    .uses_dynamic_stack: false
    .vgpr_count:     60
    .vgpr_spill_count: 0
    .wavefront_size: 64
  - .agpr_count:     0
    .args:
      - .actual_access:  read_only
        .address_space:  global
        .offset:         0
        .size:           8
        .value_kind:     global_buffer
      - .actual_access:  read_only
        .address_space:  global
        .offset:         8
        .size:           8
        .value_kind:     global_buffer
      - .address_space:  global
        .offset:         16
        .size:           8
        .value_kind:     global_buffer
      - .actual_access:  write_only
        .address_space:  global
        .offset:         24
        .size:           8
        .value_kind:     global_buffer
      - .address_space:  global
        .offset:         32
        .size:           8
        .value_kind:     global_buffer
      - .address_space:  global
        .offset:         40
        .size:           8
        .value_kind:     global_buffer
      - .actual_access:  read_only
        .address_space:  global
        .offset:         48
        .size:           8
        .value_kind:     global_buffer
      - .actual_access:  read_only
        .address_space:  global
        .offset:         56
        .size:           8
        .value_kind:     global_buffer
      - .address_space:  global
        .offset:         64
        .size:           8
        .value_kind:     global_buffer
      - .address_space:  global
        .offset:         72
        .size:           8
        .value_kind:     global_buffer
      - .actual_access:  read_only
        .address_space:  global
        .offset:         80
        .size:           8
        .value_kind:     global_buffer
      - .actual_access:  read_only
        .address_space:  global
        .offset:         88
        .size:           8
        .value_kind:     global_buffer
      - .offset:         96
        .size:           4
        .value_kind:     hidden_block_count_x
      - .offset:         100
        .size:           4
        .value_kind:     hidden_block_count_y
      - .offset:         104
        .size:           4
        .value_kind:     hidden_block_count_z
      - .offset:         108
        .size:           2
        .value_kind:     hidden_group_size_x
      - .offset:         110
        .size:           2
        .value_kind:     hidden_group_size_y
      - .offset:         112
        .size:           2
        .value_kind:     hidden_group_size_z
      - .offset:         114
        .size:           2
        .value_kind:     hidden_remainder_x
      - .offset:         116
        .size:           2
        .value_kind:     hidden_remainder_y
      - .offset:         118
        .size:           2
        .value_kind:     hidden_remainder_z
      - .offset:         136
        .size:           8
        .value_kind:     hidden_global_offset_x
      - .offset:         144
        .size:           8
        .value_kind:     hidden_global_offset_y
      - .offset:         152
        .size:           8
        .value_kind:     hidden_global_offset_z
      - .offset:         160
        .size:           2
        .value_kind:     hidden_grid_dims
    .group_segment_fixed_size: 26384
    .kernarg_segment_align: 8
    .kernarg_segment_size: 352
    .language:       OpenCL C
    .language_version:
      - 2
      - 0
    .max_flat_workgroup_size: 512
    .name:           _Z12layer_kernelILb1ELi512ELi64EEvPKDv8_DF16_PKfPS0_PiS6_S6_S2_S4_S5_PfPK15HIP_vector_typeIiLj2EEPKi
    .private_segment_fixed_size: 0
    .sgpr_count:     52
    .sgpr_spill_count: 0
    .symbol:         _Z12layer_kernelILb1ELi512ELi64EEvPKDv8_DF16_PKfPS0_PiS6_S6_S2_S4_S5_PfPK15HIP_vector_typeIiLj2EEPKi.kd
    .uniform_work_group_size: 1
    .uses_dynamic_stack: false
    .vgpr_count:     61
    .vgpr_spill_count: 0
    .wavefront_size: 64
  - .agpr_count:     0
    .args:
      - .actual_access:  read_only
        .address_space:  global
        .offset:         0
        .size:           8
        .value_kind:     global_buffer
      - .actual_access:  read_only
        .address_space:  global
        .offset:         8
        .size:           8
        .value_kind:     global_buffer
      - .actual_access:  read_only
        .address_space:  global
        .offset:         16
        .size:           8
        .value_kind:     global_buffer
      - .actual_access:  read_only
        .address_space:  global
        .offset:         24
        .size:           8
        .value_kind:     global_buffer
      - .actual_access:  read_only
        .address_space:  global
        .offset:         32
        .size:           8
        .value_kind:     global_buffer
      - .actual_access:  read_only
        .address_space:  global
        .offset:         40
        .size:           8
        .value_kind:     global_buffer
      - .actual_access:  read_only
        .address_space:  global
        .offset:         48
        .size:           8
        .value_kind:     global_buffer
      - .actual_access:  read_only
        .address_space:  global
        .offset:         56
        .size:           8
        .value_kind:     global_buffer
      - .address_space:  global
        .offset:         64
        .size:           8
        .value_kind:     global_buffer
      - .address_space:  global
        .offset:         72
        .size:           8
        .value_kind:     global_buffer
      - .actual_access:  read_only
        .address_space:  global
        .offset:         80
        .size:           8
        .value_kind:     global_buffer
      - .actual_access:  read_only
        .address_space:  global
        .offset:         88
        .size:           8
        .value_kind:     global_buffer
      - .offset:         96
        .size:           4
        .value_kind:     hidden_block_count_x
      - .offset:         100
        .size:           4
        .value_kind:     hidden_block_count_y
      - .offset:         104
        .size:           4
        .value_kind:     hidden_block_count_z
      - .offset:         108
        .size:           2
        .value_kind:     hidden_group_size_x
      - .offset:         110
        .size:           2
        .value_kind:     hidden_group_size_y
      - .offset:         112
        .size:           2
        .value_kind:     hidden_group_size_z
      - .offset:         114
        .size:           2
        .value_kind:     hidden_remainder_x
      - .offset:         116
        .size:           2
        .value_kind:     hidden_remainder_y
      - .offset:         118
        .size:           2
        .value_kind:     hidden_remainder_z
      - .offset:         136
        .size:           8
        .value_kind:     hidden_global_offset_x
      - .offset:         144
        .size:           8
        .value_kind:     hidden_global_offset_y
      - .offset:         152
        .size:           8
        .value_kind:     hidden_global_offset_z
      - .offset:         160
        .size:           2
        .value_kind:     hidden_grid_dims
    .group_segment_fixed_size: 12932
    .kernarg_segment_align: 8
    .kernarg_segment_size: 352
    .language:       OpenCL C
    .language_version:
      - 2
      - 0
    .max_flat_workgroup_size: 256
    .name:           _Z12layer_kernelILb0ELi256ELi32EEvPKDv8_DF16_PKfPS0_PiS6_S6_S2_S4_S5_PfPK15HIP_vector_typeIiLj2EEPKi
    .private_segment_fixed_size: 0
    .sgpr_count:     36
    .sgpr_spill_count: 0
    .symbol:         _Z12layer_kernelILb0ELi256ELi32EEvPKDv8_DF16_PKfPS0_PiS6_S6_S2_S4_S5_PfPK15HIP_vector_typeIiLj2EEPKi.kd
    .uniform_work_group_size: 1
    .uses_dynamic_stack: false
    .vgpr_count:     64
    .vgpr_spill_count: 0
    .wavefront_size: 64
